# grid barrier spin loops: s_sleep 1 between polls removed (waiting workgroups poll an L2-resident line now)
# speedup vs baseline: 1.0038x; 1.0038x over previous
.LBB0_176:
	global_load_dword v15, v16, s[72:73] offset:1024 sc1
	global_load_dword v0, v16, s[72:73] offset:1280 sc1
	global_load_dword v1, v16, s[72:73] offset:1536 sc1
	global_load_dword v2, v16, s[72:73] offset:1792 sc1
	global_load_dword v3, v16, s[72:73] offset:2048 sc1
	global_load_dword v4, v16, s[72:73] offset:2304 sc1
	global_load_dword v5, v16, s[72:73] offset:2560 sc1
	global_load_dword v6, v16, s[72:73] offset:2816 sc1
	global_load_dword v7, v16, s[72:73] offset:3072 sc1
	global_load_dword v8, v16, s[72:73] offset:3328 sc1
	global_load_dword v9, v16, s[72:73] offset:3584 sc1
	global_load_dword v10, v16, s[72:73] offset:3840 sc1
	global_load_dword v11, v16, s[2:3] sc1
	global_load_dword v12, v16, s[4:5] sc1
	global_load_dword v13, v16, s[6:7] sc1
	global_load_dword v14, v16, s[8:9] sc1
	s_mov_b64 s[10:11], -1
	s_mov_b64 s[12:13], -1
	s_waitcnt vmcnt(14)
	v_add_u32_e32 v17, v0, v15
	s_waitcnt vmcnt(13)
	v_add_u32_e32 v17, v17, v1
	s_waitcnt vmcnt(12)
	v_add_u32_e32 v17, v17, v2
	s_waitcnt vmcnt(11)
	v_add_u32_e32 v17, v17, v3
	s_waitcnt vmcnt(10)
	v_add_u32_e32 v17, v17, v4
	s_waitcnt vmcnt(9)
	v_add_u32_e32 v17, v17, v5
	s_waitcnt vmcnt(8)
	v_add_u32_e32 v17, v17, v6
	s_waitcnt vmcnt(7)
	v_add_u32_e32 v17, v17, v7
	s_waitcnt vmcnt(6)
	v_add_u32_e32 v17, v17, v8
	s_waitcnt vmcnt(5)
	v_add_u32_e32 v17, v17, v9
	s_waitcnt vmcnt(4)
	v_add_u32_e32 v17, v17, v10
	s_waitcnt vmcnt(3)
	v_add_u32_e32 v17, v17, v11
	s_waitcnt vmcnt(2)
	v_add_u32_e32 v17, v17, v12
	s_waitcnt vmcnt(1)
	v_add_u32_e32 v17, v17, v13
	s_waitcnt vmcnt(0)
	v_add_u32_e32 v17, v17, v14
	v_cmp_eq_u32_e32 vcc, s16, v17
	s_cbranch_vccnz .LBB0_175
	s_and_b32 s10, s17, 0xff
	s_cmp_eq_u32 s10, 0
	s_mov_b64 s[10:11], -1
	s_mov_b64 s[14:15], -1
	s_nop 0
	s_cbranch_scc1 .LBB0_180
	s_and_b64 vcc, exec, s[14:15]
	s_cbranch_vccz .LBB0_175

.LBB0_194:
	s_and_b32 s17, s16, 0xff
	s_mov_b64 s[14:15], -1
	s_cmp_lg_u32 s17, 0
	s_mov_b64 s[36:37], -1
	s_nop 0
	s_cbranch_scc0 .LBB0_197
	s_and_b64 vcc, exec, s[36:37]
	s_cbranch_vccz .LBB0_193

.LBB0_211:
	s_and_b32 s17, s16, 0xff
	s_cmp_lg_u32 s17, 0
	s_mov_b64 s[36:37], -1
	s_nop 0
	s_cbranch_scc0 .LBB0_214
	s_mov_b64 s[38:39], -1
	s_and_b64 vcc, exec, s[36:37]
	s_cbranch_vccz .LBB0_210

.LBB0_252:
	global_load_dword v15, v16, s[72:73] offset:1024 sc1
	global_load_dword v0, v16, s[72:73] offset:1280 sc1
	global_load_dword v1, v16, s[72:73] offset:1536 sc1
	global_load_dword v2, v16, s[72:73] offset:1792 sc1
	global_load_dword v3, v16, s[72:73] offset:2048 sc1
	global_load_dword v4, v16, s[72:73] offset:2304 sc1
	global_load_dword v5, v16, s[72:73] offset:2560 sc1
	global_load_dword v6, v16, s[72:73] offset:2816 sc1
	global_load_dword v7, v16, s[72:73] offset:3072 sc1
	global_load_dword v8, v16, s[72:73] offset:3328 sc1
	global_load_dword v9, v16, s[72:73] offset:3584 sc1
	global_load_dword v10, v16, s[72:73] offset:3840 sc1
	global_load_dword v11, v16, s[2:3] sc1
	global_load_dword v12, v16, s[6:7] sc1
	global_load_dword v13, v16, s[8:9] sc1
	global_load_dword v14, v16, s[10:11] sc1
	s_mov_b64 s[12:13], -1
	s_mov_b64 s[14:15], -1
	s_waitcnt vmcnt(14)
	v_add_u32_e32 v17, v0, v15
	s_waitcnt vmcnt(13)
	v_add_u32_e32 v17, v17, v1
	s_waitcnt vmcnt(12)
	v_add_u32_e32 v17, v17, v2
	s_waitcnt vmcnt(11)
	v_add_u32_e32 v17, v17, v3
	s_waitcnt vmcnt(10)
	v_add_u32_e32 v17, v17, v4
	s_waitcnt vmcnt(9)
	v_add_u32_e32 v17, v17, v5
	s_waitcnt vmcnt(8)
	v_add_u32_e32 v17, v17, v6
	s_waitcnt vmcnt(7)
	v_add_u32_e32 v17, v17, v7
	s_waitcnt vmcnt(6)
	v_add_u32_e32 v17, v17, v8
	s_waitcnt vmcnt(5)
	v_add_u32_e32 v17, v17, v9
	s_waitcnt vmcnt(4)
	v_add_u32_e32 v17, v17, v10
	s_waitcnt vmcnt(3)
	v_add_u32_e32 v17, v17, v11
	s_waitcnt vmcnt(2)
	v_add_u32_e32 v17, v17, v12
	s_waitcnt vmcnt(1)
	v_add_u32_e32 v17, v17, v13
	s_waitcnt vmcnt(0)
	v_add_u32_e32 v17, v17, v14
	v_cmp_eq_u32_e32 vcc, s16, v17
	s_cbranch_vccnz .LBB0_251
	s_and_b32 s12, s17, 0xff
	s_cmp_eq_u32 s12, 0
	s_mov_b64 s[12:13], -1
	s_mov_b64 s[34:35], -1
	s_nop 0
	s_cbranch_scc1 .LBB0_256
	s_and_b64 vcc, exec, s[34:35]
	s_cbranch_vccz .LBB0_251

.LBB0_270:
	s_and_b32 s17, s16, 0xff
	s_mov_b64 s[34:35], -1
	s_cmp_lg_u32 s17, 0
	s_mov_b64 s[38:39], -1
	s_nop 0
	s_cbranch_scc0 .LBB0_273
	s_and_b64 vcc, exec, s[38:39]
	s_cbranch_vccz .LBB0_269

.LBB0_287:
	s_and_b32 s17, s16, 0xff
	s_cmp_lg_u32 s17, 0
	s_mov_b64 s[38:39], -1
	s_nop 0
	s_cbranch_scc0 .LBB0_290
	s_mov_b64 s[40:41], -1
	s_and_b64 vcc, exec, s[38:39]
	s_cbranch_vccz .LBB0_286

.LBB0_540:
	s_and_b32 s17, s16, 0xff
	s_mov_b64 s[14:15], -1
	s_cmp_lg_u32 s17, 0
	s_mov_b64 s[26:27], -1
	s_nop 0
	s_cbranch_scc0 .LBB0_543
	s_and_b64 vcc, exec, s[26:27]
	s_cbranch_vccz .LBB0_539

.LBB0_557:
	s_and_b32 s17, s16, 0xff
	s_cmp_lg_u32 s17, 0
	s_mov_b64 s[26:27], -1
	s_nop 0
	s_cbranch_scc0 .LBB0_560
	s_mov_b64 s[34:35], -1
	s_and_b64 vcc, exec, s[26:27]
	s_cbranch_vccz .LBB0_556

.LBB0_676:
	global_load_dword v15, v16, s[72:73] offset:1024 sc1
	global_load_dword v0, v16, s[72:73] offset:1280 sc1
	global_load_dword v1, v16, s[72:73] offset:1536 sc1
	global_load_dword v2, v16, s[72:73] offset:1792 sc1
	global_load_dword v3, v16, s[72:73] offset:2048 sc1
	global_load_dword v4, v16, s[72:73] offset:2304 sc1
	global_load_dword v5, v16, s[72:73] offset:2560 sc1
	global_load_dword v6, v16, s[72:73] offset:2816 sc1
	global_load_dword v7, v16, s[72:73] offset:3072 sc1
	global_load_dword v8, v16, s[72:73] offset:3328 sc1
	global_load_dword v9, v16, s[72:73] offset:3584 sc1
	global_load_dword v10, v16, s[72:73] offset:3840 sc1
	global_load_dword v11, v16, s[2:3] sc1
	global_load_dword v12, v16, s[4:5] sc1
	global_load_dword v13, v16, s[6:7] sc1
	global_load_dword v14, v16, s[10:11] sc1
	s_mov_b64 s[12:13], -1
	s_mov_b64 s[14:15], -1
	s_waitcnt vmcnt(14)
	v_add_u32_e32 v17, v0, v15
	s_waitcnt vmcnt(13)
	v_add_u32_e32 v17, v17, v1
	s_waitcnt vmcnt(12)
	v_add_u32_e32 v17, v17, v2
	s_waitcnt vmcnt(11)
	v_add_u32_e32 v17, v17, v3
	s_waitcnt vmcnt(10)
	v_add_u32_e32 v17, v17, v4
	s_waitcnt vmcnt(9)
	v_add_u32_e32 v17, v17, v5
	s_waitcnt vmcnt(8)
	v_add_u32_e32 v17, v17, v6
	s_waitcnt vmcnt(7)
	v_add_u32_e32 v17, v17, v7
	s_waitcnt vmcnt(6)
	v_add_u32_e32 v17, v17, v8
	s_waitcnt vmcnt(5)
	v_add_u32_e32 v17, v17, v9
	s_waitcnt vmcnt(4)
	v_add_u32_e32 v17, v17, v10
	s_waitcnt vmcnt(3)
	v_add_u32_e32 v17, v17, v11
	s_waitcnt vmcnt(2)
	v_add_u32_e32 v17, v17, v12
	s_waitcnt vmcnt(1)
	v_add_u32_e32 v17, v17, v13
	s_waitcnt vmcnt(0)
	v_add_u32_e32 v17, v17, v14
	v_cmp_eq_u32_e32 vcc, s18, v17
	s_cbranch_vccnz .LBB0_675
	s_and_b32 s12, s19, 0xff
	s_cmp_eq_u32 s12, 0
	s_mov_b64 s[12:13], -1
	s_mov_b64 s[16:17], -1
	s_nop 0
	s_cbranch_scc1 .LBB0_680
	s_and_b64 vcc, exec, s[16:17]
	s_cbranch_vccz .LBB0_675

.LBB0_694:
	s_and_b32 s19, s18, 0xff
	s_mov_b64 s[16:17], -1
	s_cmp_lg_u32 s19, 0
	s_mov_b64 s[26:27], -1
	s_nop 0
	s_cbranch_scc0 .LBB0_697
	s_and_b64 vcc, exec, s[26:27]
	s_cbranch_vccz .LBB0_693

.LBB0_711:
	s_and_b32 s19, s18, 0xff
	s_cmp_lg_u32 s19, 0
	s_mov_b64 s[26:27], -1
	s_nop 0
	s_cbranch_scc0 .LBB0_714
	s_mov_b64 s[34:35], -1
	s_and_b64 vcc, exec, s[26:27]
	s_cbranch_vccz .LBB0_710

.LBB0_746:
	global_load_dword v15, v16, s[72:73] offset:1024 sc1
	global_load_dword v0, v16, s[72:73] offset:1280 sc1
	global_load_dword v1, v16, s[72:73] offset:1536 sc1
	global_load_dword v2, v16, s[72:73] offset:1792 sc1
	global_load_dword v3, v16, s[72:73] offset:2048 sc1
	global_load_dword v4, v16, s[72:73] offset:2304 sc1
	global_load_dword v5, v16, s[72:73] offset:2560 sc1
	global_load_dword v6, v16, s[72:73] offset:2816 sc1
	global_load_dword v7, v16, s[72:73] offset:3072 sc1
	global_load_dword v8, v16, s[72:73] offset:3328 sc1
	global_load_dword v9, v16, s[72:73] offset:3584 sc1
	global_load_dword v10, v16, s[72:73] offset:3840 sc1
	global_load_dword v11, v16, s[2:3] sc1
	global_load_dword v12, v16, s[4:5] sc1
	global_load_dword v13, v16, s[6:7] sc1
	global_load_dword v14, v16, s[12:13] sc1
	s_mov_b64 s[14:15], -1
	s_mov_b64 s[16:17], -1
	s_waitcnt vmcnt(14)
	v_add_u32_e32 v17, v0, v15
	s_waitcnt vmcnt(13)
	v_add_u32_e32 v17, v17, v1
	s_waitcnt vmcnt(12)
	v_add_u32_e32 v17, v17, v2
	s_waitcnt vmcnt(11)
	v_add_u32_e32 v17, v17, v3
	s_waitcnt vmcnt(10)
	v_add_u32_e32 v17, v17, v4
	s_waitcnt vmcnt(9)
	v_add_u32_e32 v17, v17, v5
	s_waitcnt vmcnt(8)
	v_add_u32_e32 v17, v17, v6
	s_waitcnt vmcnt(7)
	v_add_u32_e32 v17, v17, v7
	s_waitcnt vmcnt(6)
	v_add_u32_e32 v17, v17, v8
	s_waitcnt vmcnt(5)
	v_add_u32_e32 v17, v17, v9
	s_waitcnt vmcnt(4)
	v_add_u32_e32 v17, v17, v10
	s_waitcnt vmcnt(3)
	v_add_u32_e32 v17, v17, v11
	s_waitcnt vmcnt(2)
	v_add_u32_e32 v17, v17, v12
	s_waitcnt vmcnt(1)
	v_add_u32_e32 v17, v17, v13
	s_waitcnt vmcnt(0)
	v_add_u32_e32 v17, v17, v14
	v_cmp_eq_u32_e32 vcc, s18, v17
	s_cbranch_vccnz .LBB0_745
	s_and_b32 s14, s19, 0xff
	s_cmp_eq_u32 s14, 0
	s_mov_b64 s[14:15], -1
	s_mov_b64 s[24:25], -1
	s_nop 0
	s_cbranch_scc1 .LBB0_750
	s_and_b64 vcc, exec, s[24:25]
	s_cbranch_vccz .LBB0_745

.LBB0_764:
	s_and_b32 s19, s18, 0xff
	s_mov_b64 s[24:25], -1
	s_cmp_lg_u32 s19, 0
	s_mov_b64 s[34:35], -1
	s_nop 0
	s_cbranch_scc0 .LBB0_767
	s_and_b64 vcc, exec, s[34:35]
	s_cbranch_vccz .LBB0_763

.LBB0_781:
	s_and_b32 s19, s18, 0xff
	s_cmp_lg_u32 s19, 0
	s_mov_b64 s[34:35], -1
	s_nop 0
	s_cbranch_scc0 .LBB0_784
	s_mov_b64 s[36:37], -1
	s_and_b64 vcc, exec, s[34:35]
	s_cbranch_vccz .LBB0_780

.LBB0_844:
	global_load_dword v15, v16, s[72:73] offset:1024 sc1
	global_load_dword v0, v16, s[72:73] offset:1280 sc1
	global_load_dword v1, v16, s[72:73] offset:1536 sc1
	global_load_dword v2, v16, s[72:73] offset:1792 sc1
	global_load_dword v3, v16, s[72:73] offset:2048 sc1
	global_load_dword v4, v16, s[72:73] offset:2304 sc1
	global_load_dword v5, v16, s[72:73] offset:2560 sc1
	global_load_dword v6, v16, s[72:73] offset:2816 sc1
	global_load_dword v7, v16, s[72:73] offset:3072 sc1
	global_load_dword v8, v16, s[72:73] offset:3328 sc1
	global_load_dword v9, v16, s[72:73] offset:3584 sc1
	global_load_dword v10, v16, s[72:73] offset:3840 sc1
	global_load_dword v11, v16, s[2:3] sc1
	global_load_dword v12, v16, s[4:5] sc1
	global_load_dword v13, v16, s[12:13] sc1
	global_load_dword v14, v16, s[14:15] sc1
	s_mov_b64 s[16:17], -1
	s_mov_b64 s[24:25], -1
	s_waitcnt vmcnt(14)
	v_add_u32_e32 v17, v0, v15
	s_waitcnt vmcnt(13)
	v_add_u32_e32 v17, v17, v1
	s_waitcnt vmcnt(12)
	v_add_u32_e32 v17, v17, v2
	s_waitcnt vmcnt(11)
	v_add_u32_e32 v17, v17, v3
	s_waitcnt vmcnt(10)
	v_add_u32_e32 v17, v17, v4
	s_waitcnt vmcnt(9)
	v_add_u32_e32 v17, v17, v5
	s_waitcnt vmcnt(8)
	v_add_u32_e32 v17, v17, v6
	s_waitcnt vmcnt(7)
	v_add_u32_e32 v17, v17, v7
	s_waitcnt vmcnt(6)
	v_add_u32_e32 v17, v17, v8
	s_waitcnt vmcnt(5)
	v_add_u32_e32 v17, v17, v9
	s_waitcnt vmcnt(4)
	v_add_u32_e32 v17, v17, v10
	s_waitcnt vmcnt(3)
	v_add_u32_e32 v17, v17, v11
	s_waitcnt vmcnt(2)
	v_add_u32_e32 v17, v17, v12
	s_waitcnt vmcnt(1)
	v_add_u32_e32 v17, v17, v13
	s_waitcnt vmcnt(0)
	v_add_u32_e32 v17, v17, v14
	v_cmp_eq_u32_e32 vcc, s18, v17
	s_cbranch_vccnz .LBB0_843
	s_and_b32 s16, s19, 0xff
	s_cmp_eq_u32 s16, 0
	s_mov_b64 s[16:17], -1
	s_mov_b64 s[26:27], -1
	s_nop 0
	s_cbranch_scc1 .LBB0_848
	s_and_b64 vcc, exec, s[26:27]
	s_cbranch_vccz .LBB0_843

.LBB0_862:
	s_and_b32 s19, s18, 0xff
	s_mov_b64 s[26:27], -1
	s_cmp_lg_u32 s19, 0
	s_mov_b64 s[36:37], -1
	s_nop 0
	s_cbranch_scc0 .LBB0_865
	s_and_b64 vcc, exec, s[36:37]
	s_cbranch_vccz .LBB0_861

.LBB0_879:
	s_and_b32 s19, s18, 0xff
	s_cmp_lg_u32 s19, 0
	s_mov_b64 s[36:37], -1
	s_nop 0
	s_cbranch_scc0 .LBB0_882
	s_mov_b64 s[38:39], -1
	s_and_b64 vcc, exec, s[36:37]
	s_cbranch_vccz .LBB0_878

.LBB0_934:
	global_load_dword v15, v16, s[72:73] offset:1024 sc1
	global_load_dword v0, v16, s[72:73] offset:1280 sc1
	global_load_dword v1, v16, s[72:73] offset:1536 sc1
	global_load_dword v2, v16, s[72:73] offset:1792 sc1
	global_load_dword v3, v16, s[72:73] offset:2048 sc1
	global_load_dword v4, v16, s[72:73] offset:2304 sc1
	global_load_dword v5, v16, s[72:73] offset:2560 sc1
	global_load_dword v6, v16, s[72:73] offset:2816 sc1
	global_load_dword v7, v16, s[72:73] offset:3072 sc1
	global_load_dword v8, v16, s[72:73] offset:3328 sc1
	global_load_dword v9, v16, s[72:73] offset:3584 sc1
	global_load_dword v10, v16, s[72:73] offset:3840 sc1
	global_load_dword v11, v16, s[4:5] sc1
	global_load_dword v12, v16, s[6:7] sc1
	global_load_dword v13, v16, s[12:13] sc1
	global_load_dword v14, v16, s[14:15] sc1
	s_mov_b64 s[16:17], -1
	s_mov_b64 s[24:25], -1
	s_waitcnt vmcnt(14)
	v_add_u32_e32 v17, v0, v15
	s_waitcnt vmcnt(13)
	v_add_u32_e32 v17, v17, v1
	s_waitcnt vmcnt(12)
	v_add_u32_e32 v17, v17, v2
	s_waitcnt vmcnt(11)
	v_add_u32_e32 v17, v17, v3
	s_waitcnt vmcnt(10)
	v_add_u32_e32 v17, v17, v4
	s_waitcnt vmcnt(9)
	v_add_u32_e32 v17, v17, v5
	s_waitcnt vmcnt(8)
	v_add_u32_e32 v17, v17, v6
	s_waitcnt vmcnt(7)
	v_add_u32_e32 v17, v17, v7
	s_waitcnt vmcnt(6)
	v_add_u32_e32 v17, v17, v8
	s_waitcnt vmcnt(5)
	v_add_u32_e32 v17, v17, v9
	s_waitcnt vmcnt(4)
	v_add_u32_e32 v17, v17, v10
	s_waitcnt vmcnt(3)
	v_add_u32_e32 v17, v17, v11
	s_waitcnt vmcnt(2)
	v_add_u32_e32 v17, v17, v12
	s_waitcnt vmcnt(1)
	v_add_u32_e32 v17, v17, v13
	s_waitcnt vmcnt(0)
	v_add_u32_e32 v17, v17, v14
	v_cmp_eq_u32_e32 vcc, s18, v17
	s_cbranch_vccnz .LBB0_933
	s_and_b32 s16, s19, 0xff
	s_cmp_eq_u32 s16, 0
	s_mov_b64 s[16:17], -1
	s_mov_b64 s[26:27], -1
	s_nop 0
	s_cbranch_scc1 .LBB0_938
	s_and_b64 vcc, exec, s[26:27]
	s_cbranch_vccz .LBB0_933

.LBB0_1132:
	s_and_b32 s16, s18, 0xff
	s_mov_b64 s[14:15], -1
	s_cmp_lg_u32 s16, 0
	s_mov_b64 s[24:25], -1
	s_nop 0
	s_cbranch_scc0 .LBB0_1135
	s_and_b64 vcc, exec, s[24:25]
	s_cbranch_vccz .LBB0_1131

.LBB0_1149:
	s_and_b32 s16, s18, 0xff
	s_cmp_lg_u32 s16, 0
	s_mov_b64 s[24:25], -1
	s_nop 0
	s_cbranch_scc0 .LBB0_1152
	s_mov_b64 s[26:27], -1
	s_and_b64 vcc, exec, s[24:25]
	s_cbranch_vccz .LBB0_1148

.LBB0_1571:
	s_and_b32 s16, s18, 0xff
	s_mov_b64 s[14:15], -1
	s_cmp_lg_u32 s16, 0
	s_mov_b64 s[28:29], -1
	s_nop 0
	s_cbranch_scc0 .LBB0_1574
	s_and_b64 vcc, exec, s[28:29]
	s_cbranch_vccz .LBB0_1570

.LBB0_1588:
	s_and_b32 s16, s18, 0xff
	s_cmp_lg_u32 s16, 0
	s_mov_b64 s[28:29], -1
	s_nop 0
	s_cbranch_scc0 .LBB0_1591
	s_mov_b64 s[30:31], -1
	s_and_b64 vcc, exec, s[28:29]
	s_cbranch_vccz .LBB0_1587

.LBB0_1641:
	s_and_b32 s16, s18, 0xff
	s_mov_b64 s[14:15], -1
	s_cmp_lg_u32 s16, 0
	s_mov_b64 s[30:31], -1
	s_nop 0
	s_cbranch_scc0 .LBB0_1644
	s_and_b64 vcc, exec, s[30:31]
	s_cbranch_vccz .LBB0_1640

.LBB0_1658:
	s_and_b32 s16, s18, 0xff
	s_cmp_lg_u32 s16, 0
	s_mov_b64 s[30:31], -1
	s_nop 0
	s_cbranch_scc0 .LBB0_1661
	s_mov_b64 s[34:35], -1
	s_and_b64 vcc, exec, s[30:31]
	s_cbranch_vccz .LBB0_1657

.LBB0_1721:
	global_load_dword v15, v16, s[72:73] offset:1024 sc1
	global_load_dword v0, v16, s[72:73] offset:1280 sc1
	global_load_dword v1, v16, s[72:73] offset:1536 sc1
	global_load_dword v2, v16, s[72:73] offset:1792 sc1
	global_load_dword v3, v16, s[72:73] offset:2048 sc1
	global_load_dword v4, v16, s[72:73] offset:2304 sc1
	global_load_dword v5, v16, s[72:73] offset:2560 sc1
	global_load_dword v6, v16, s[72:73] offset:2816 sc1
	global_load_dword v7, v16, s[72:73] offset:3072 sc1
	global_load_dword v8, v16, s[72:73] offset:3328 sc1
	global_load_dword v9, v16, s[72:73] offset:3584 sc1
	global_load_dword v10, v16, s[72:73] offset:3840 sc1
	global_load_dword v11, v16, s[2:3] sc1
	global_load_dword v12, v16, s[4:5] sc1
	global_load_dword v13, v16, s[8:9] sc1
	global_load_dword v14, v16, s[10:11] sc1
	s_mov_b64 s[12:13], -1
	s_mov_b64 s[14:15], -1
	s_waitcnt vmcnt(14)
	v_add_u32_e32 v17, v0, v15
	s_waitcnt vmcnt(13)
	v_add_u32_e32 v17, v17, v1
	s_waitcnt vmcnt(12)
	v_add_u32_e32 v17, v17, v2
	s_waitcnt vmcnt(11)
	v_add_u32_e32 v17, v17, v3
	s_waitcnt vmcnt(10)
	v_add_u32_e32 v17, v17, v4
	s_waitcnt vmcnt(9)
	v_add_u32_e32 v17, v17, v5
	s_waitcnt vmcnt(8)
	v_add_u32_e32 v17, v17, v6
	s_waitcnt vmcnt(7)
	v_add_u32_e32 v17, v17, v7
	s_waitcnt vmcnt(6)
	v_add_u32_e32 v17, v17, v8
	s_waitcnt vmcnt(5)
	v_add_u32_e32 v17, v17, v9
	s_waitcnt vmcnt(4)
	v_add_u32_e32 v17, v17, v10
	s_waitcnt vmcnt(3)
	v_add_u32_e32 v17, v17, v11
	s_waitcnt vmcnt(2)
	v_add_u32_e32 v17, v17, v12
	s_waitcnt vmcnt(1)
	v_add_u32_e32 v17, v17, v13
	s_waitcnt vmcnt(0)
	v_add_u32_e32 v17, v17, v14
	v_cmp_eq_u32_e32 vcc, s18, v17
	s_cbranch_vccnz .LBB0_1720
	s_and_b32 s12, s19, 0xff
	s_cmp_eq_u32 s12, 0
	s_mov_b64 s[12:13], -1
	s_mov_b64 s[16:17], -1
	s_nop 0
	s_cbranch_scc1 .LBB0_1725
	s_and_b64 vcc, exec, s[16:17]
	s_cbranch_vccz .LBB0_1720

.LBB0_1739:
	s_and_b32 s19, s18, 0xff
	s_mov_b64 s[16:17], -1
	s_cmp_lg_u32 s19, 0
	s_mov_b64 s[34:35], -1
	s_nop 0
	s_cbranch_scc0 .LBB0_1742
	s_and_b64 vcc, exec, s[34:35]
	s_cbranch_vccz .LBB0_1738

.LBB0_1811:
	global_load_dword v15, v16, s[72:73] offset:1024 sc1
	global_load_dword v0, v16, s[72:73] offset:1280 sc1
	global_load_dword v1, v16, s[72:73] offset:1536 sc1
	global_load_dword v2, v16, s[72:73] offset:1792 sc1
	global_load_dword v3, v16, s[72:73] offset:2048 sc1
	global_load_dword v4, v16, s[72:73] offset:2304 sc1
	global_load_dword v5, v16, s[72:73] offset:2560 sc1
	global_load_dword v6, v16, s[72:73] offset:2816 sc1
	global_load_dword v7, v16, s[72:73] offset:3072 sc1
	global_load_dword v8, v16, s[72:73] offset:3328 sc1
	global_load_dword v9, v16, s[72:73] offset:3584 sc1
	global_load_dword v10, v16, s[72:73] offset:3840 sc1
	global_load_dword v11, v16, s[4:5] sc1
	global_load_dword v12, v16, s[6:7] sc1
	global_load_dword v13, v16, s[8:9] sc1
	global_load_dword v14, v16, s[10:11] sc1
	s_mov_b64 s[12:13], -1
	s_mov_b64 s[14:15], -1
	s_waitcnt vmcnt(14)
	v_add_u32_e32 v17, v0, v15
	s_waitcnt vmcnt(13)
	v_add_u32_e32 v17, v17, v1
	s_waitcnt vmcnt(12)
	v_add_u32_e32 v17, v17, v2
	s_waitcnt vmcnt(11)
	v_add_u32_e32 v17, v17, v3
	s_waitcnt vmcnt(10)
	v_add_u32_e32 v17, v17, v4
	s_waitcnt vmcnt(9)
	v_add_u32_e32 v17, v17, v5
	s_waitcnt vmcnt(8)
	v_add_u32_e32 v17, v17, v6
	s_waitcnt vmcnt(7)
	v_add_u32_e32 v17, v17, v7
	s_waitcnt vmcnt(6)
	v_add_u32_e32 v17, v17, v8
	s_waitcnt vmcnt(5)
	v_add_u32_e32 v17, v17, v9
	s_waitcnt vmcnt(4)
	v_add_u32_e32 v17, v17, v10
	s_waitcnt vmcnt(3)
	v_add_u32_e32 v17, v17, v11
	s_waitcnt vmcnt(2)
	v_add_u32_e32 v17, v17, v12
	s_waitcnt vmcnt(1)
	v_add_u32_e32 v17, v17, v13
	s_waitcnt vmcnt(0)
	v_add_u32_e32 v17, v17, v14
	v_cmp_eq_u32_e32 vcc, s18, v17
	s_cbranch_vccnz .LBB0_1810
	s_and_b32 s12, s19, 0xff
	s_cmp_eq_u32 s12, 0
	s_mov_b64 s[12:13], -1
	s_mov_b64 s[16:17], -1
	s_nop 0
	s_cbranch_scc1 .LBB0_1815
	s_and_b64 vcc, exec, s[16:17]
	s_cbranch_vccz .LBB0_1810

.LBB0_2331:
	s_and_b32 s16, s20, 0xff
	s_mov_b64 s[14:15], -1
	s_cmp_lg_u32 s16, 0
	s_mov_b64 s[18:19], -1
	s_nop 0
	s_cbranch_scc0 .LBB0_2334
	s_and_b64 vcc, exec, s[18:19]
	s_cbranch_vccz .LBB0_2330

.LBB0_2348:
	s_and_b32 s16, s22, 0xff
	s_cmp_lg_u32 s16, 0
	s_mov_b64 s[18:19], -1
	s_nop 0
	s_cbranch_scc0 .LBB0_2351
	s_mov_b64 s[20:21], -1
	s_and_b64 vcc, exec, s[18:19]
	s_cbranch_vccz .LBB0_2347

.LBB0_2450:
	s_and_b32 s16, s24, 0xff
	s_mov_b64 s[14:15], -1
	s_cmp_lg_u32 s16, 0
	s_mov_b64 s[22:23], -1
	s_nop 0
	s_cbranch_scc0 .LBB0_2453
	s_and_b64 vcc, exec, s[22:23]
	s_cbranch_vccz .LBB0_2449

.LBB0_2467:
	s_and_b32 s16, s26, 0xff
	s_cmp_lg_u32 s16, 0
	s_mov_b64 s[22:23], -1
	s_nop 0
	s_cbranch_scc0 .LBB0_2470
	s_mov_b64 s[24:25], -1
	s_and_b64 vcc, exec, s[22:23]
	s_cbranch_vccz .LBB0_2466

.LBB0_2520:
	s_and_b32 s16, s26, 0xff
	s_mov_b64 s[14:15], -1
	s_cmp_lg_u32 s16, 0
	s_mov_b64 s[24:25], -1
	s_nop 0
	s_cbranch_scc0 .LBB0_2523
	s_and_b64 vcc, exec, s[24:25]
	s_cbranch_vccz .LBB0_2519

.LBB0_2537:
	s_and_b32 s16, s28, 0xff
	s_cmp_lg_u32 s16, 0
	s_mov_b64 s[24:25], -1
	s_nop 0
	s_cbranch_scc0 .LBB0_2540
	s_mov_b64 s[26:27], -1
	s_and_b64 vcc, exec, s[24:25]
	s_cbranch_vccz .LBB0_2536

.LBB0_2600:
	global_load_dword v15, v16, s[72:73] offset:1024 sc1
	global_load_dword v0, v16, s[72:73] offset:1280 sc1
	global_load_dword v1, v16, s[72:73] offset:1536 sc1
	global_load_dword v2, v16, s[72:73] offset:1792 sc1
	global_load_dword v3, v16, s[72:73] offset:2048 sc1
	global_load_dword v4, v16, s[72:73] offset:2304 sc1
	global_load_dword v5, v16, s[72:73] offset:2560 sc1
	global_load_dword v6, v16, s[72:73] offset:2816 sc1
	global_load_dword v7, v16, s[72:73] offset:3072 sc1
	global_load_dword v8, v16, s[72:73] offset:3328 sc1
	global_load_dword v9, v16, s[72:73] offset:3584 sc1
	global_load_dword v10, v16, s[72:73] offset:3840 sc1
	global_load_dword v11, v16, s[2:3] sc1
	global_load_dword v12, v16, s[4:5] sc1
	global_load_dword v13, v16, s[8:9] sc1
	global_load_dword v14, v16, s[10:11] sc1
	s_mov_b64 s[12:13], -1
	s_mov_b64 s[14:15], -1
	s_waitcnt vmcnt(14)
	v_add_u32_e32 v17, v0, v15
	s_waitcnt vmcnt(13)
	v_add_u32_e32 v17, v17, v1
	s_waitcnt vmcnt(12)
	v_add_u32_e32 v17, v17, v2
	s_waitcnt vmcnt(11)
	v_add_u32_e32 v17, v17, v3
	s_waitcnt vmcnt(10)
	v_add_u32_e32 v17, v17, v4
	s_waitcnt vmcnt(9)
	v_add_u32_e32 v17, v17, v5
	s_waitcnt vmcnt(8)
	v_add_u32_e32 v17, v17, v6
	s_waitcnt vmcnt(7)
	v_add_u32_e32 v17, v17, v7
	s_waitcnt vmcnt(6)
	v_add_u32_e32 v17, v17, v8
	s_waitcnt vmcnt(5)
	v_add_u32_e32 v17, v17, v9
	s_waitcnt vmcnt(4)
	v_add_u32_e32 v17, v17, v10
	s_waitcnt vmcnt(3)
	v_add_u32_e32 v17, v17, v11
	s_waitcnt vmcnt(2)
	v_add_u32_e32 v17, v17, v12
	s_waitcnt vmcnt(1)
	v_add_u32_e32 v17, v17, v13
	s_waitcnt vmcnt(0)
	v_add_u32_e32 v17, v17, v14
	v_cmp_eq_u32_e32 vcc, s24, v17
	s_cbranch_vccnz .LBB0_2599
	s_and_b32 s12, s25, 0xff
	s_cmp_eq_u32 s12, 0
	s_mov_b64 s[12:13], -1
	s_mov_b64 s[16:17], -1
	s_nop 0
	s_cbranch_scc1 .LBB0_2604
	s_and_b64 vcc, exec, s[16:17]
	s_cbranch_vccz .LBB0_2599

.LBB0_2618:
	s_and_b32 s24, s28, 0xff
	s_mov_b64 s[16:17], -1
	s_cmp_lg_u32 s24, 0
	s_mov_b64 s[26:27], -1
	s_nop 0
	s_cbranch_scc0 .LBB0_2621
	s_and_b64 vcc, exec, s[26:27]
	s_cbranch_vccz .LBB0_2617

.LBB0_2635:
	s_and_b32 s24, s30, 0xff
	s_cmp_lg_u32 s24, 0
	s_mov_b64 s[26:27], -1
	s_nop 0
	s_cbranch_scc0 .LBB0_2638
	s_mov_b64 s[28:29], -1
	s_and_b64 vcc, exec, s[26:27]
	s_cbranch_vccz .LBB0_2634

.LBB0_2690:
	global_load_dword v15, v16, s[72:73] offset:1024 sc1
	global_load_dword v0, v16, s[72:73] offset:1280 sc1
	global_load_dword v1, v16, s[72:73] offset:1536 sc1
	global_load_dword v2, v16, s[72:73] offset:1792 sc1
	global_load_dword v3, v16, s[72:73] offset:2048 sc1
	global_load_dword v4, v16, s[72:73] offset:2304 sc1
	global_load_dword v5, v16, s[72:73] offset:2560 sc1
	global_load_dword v6, v16, s[72:73] offset:2816 sc1
	global_load_dword v7, v16, s[72:73] offset:3072 sc1
	global_load_dword v8, v16, s[72:73] offset:3328 sc1
	global_load_dword v9, v16, s[72:73] offset:3584 sc1
	global_load_dword v10, v16, s[72:73] offset:3840 sc1
	global_load_dword v11, v16, s[4:5] sc1
	global_load_dword v12, v16, s[6:7] sc1
	global_load_dword v13, v16, s[8:9] sc1
	global_load_dword v14, v16, s[10:11] sc1
	s_mov_b64 s[12:13], -1
	s_mov_b64 s[14:15], -1
	s_waitcnt vmcnt(14)
	v_add_u32_e32 v17, v0, v15
	s_waitcnt vmcnt(13)
	v_add_u32_e32 v17, v17, v1
	s_waitcnt vmcnt(12)
	v_add_u32_e32 v17, v17, v2
	s_waitcnt vmcnt(11)
	v_add_u32_e32 v17, v17, v3
	s_waitcnt vmcnt(10)
	v_add_u32_e32 v17, v17, v4
	s_waitcnt vmcnt(9)
	v_add_u32_e32 v17, v17, v5
	s_waitcnt vmcnt(8)
	v_add_u32_e32 v17, v17, v6
	s_waitcnt vmcnt(7)
	v_add_u32_e32 v17, v17, v7
	s_waitcnt vmcnt(6)
	v_add_u32_e32 v17, v17, v8
	s_waitcnt vmcnt(5)
	v_add_u32_e32 v17, v17, v9
	s_waitcnt vmcnt(4)
	v_add_u32_e32 v17, v17, v10
	s_waitcnt vmcnt(3)
	v_add_u32_e32 v17, v17, v11
	s_waitcnt vmcnt(2)
	v_add_u32_e32 v17, v17, v12
	s_waitcnt vmcnt(1)
	v_add_u32_e32 v17, v17, v13
	s_waitcnt vmcnt(0)
	v_add_u32_e32 v17, v17, v14
	v_cmp_eq_u32_e32 vcc, s24, v17
	s_cbranch_vccnz .LBB0_2689
	s_and_b32 s12, s25, 0xff
	s_cmp_eq_u32 s12, 0
	s_mov_b64 s[12:13], -1
	s_mov_b64 s[16:17], -1
	s_nop 0
	s_cbranch_scc1 .LBB0_2694
	s_and_b64 vcc, exec, s[16:17]
	s_cbranch_vccz .LBB0_2689

.LBB0_2966:
	s_and_b32 s18, s22, 0xff
	s_mov_b64 s[16:17], -1
	s_cmp_lg_u32 s18, 0
	s_mov_b64 s[20:21], -1
	s_nop 0
	s_cbranch_scc0 .LBB0_2969
	s_and_b64 vcc, exec, s[20:21]
	s_cbranch_vccz .LBB0_2965

.LBB0_2983:
	s_and_b32 s18, s24, 0xff
	s_cmp_lg_u32 s18, 0
	s_mov_b64 s[20:21], -1
	s_nop 0
	s_cbranch_scc0 .LBB0_2986
	s_mov_b64 s[22:23], -1
	s_and_b64 vcc, exec, s[20:21]
	s_cbranch_vccz .LBB0_2982

.LBB0_3180:
	global_load_dword v15, v16, s[72:73] offset:1024 sc1
	global_load_dword v0, v16, s[72:73] offset:1280 sc1
	global_load_dword v1, v16, s[72:73] offset:1536 sc1
	global_load_dword v2, v16, s[72:73] offset:1792 sc1
	global_load_dword v3, v16, s[72:73] offset:2048 sc1
	global_load_dword v4, v16, s[72:73] offset:2304 sc1
	global_load_dword v5, v16, s[72:73] offset:2560 sc1
	global_load_dword v6, v16, s[72:73] offset:2816 sc1
	global_load_dword v7, v16, s[72:73] offset:3072 sc1
	global_load_dword v8, v16, s[72:73] offset:3328 sc1
	global_load_dword v9, v16, s[72:73] offset:3584 sc1
	global_load_dword v10, v16, s[72:73] offset:3840 sc1
	global_load_dword v11, v16, s[2:3] sc1
	global_load_dword v12, v16, s[4:5] sc1
	global_load_dword v13, v16, s[6:7] sc1
	global_load_dword v14, v16, s[10:11] sc1
	s_mov_b64 s[12:13], -1
	s_mov_b64 s[14:15], -1
	s_waitcnt vmcnt(14)
	v_add_u32_e32 v17, v0, v15
	s_waitcnt vmcnt(13)
	v_add_u32_e32 v17, v17, v1
	s_waitcnt vmcnt(12)
	v_add_u32_e32 v17, v17, v2
	s_waitcnt vmcnt(11)
	v_add_u32_e32 v17, v17, v3
	s_waitcnt vmcnt(10)
	v_add_u32_e32 v17, v17, v4
	s_waitcnt vmcnt(9)
	v_add_u32_e32 v17, v17, v5
	s_waitcnt vmcnt(8)
	v_add_u32_e32 v17, v17, v6
	s_waitcnt vmcnt(7)
	v_add_u32_e32 v17, v17, v7
	s_waitcnt vmcnt(6)
	v_add_u32_e32 v17, v17, v8
	s_waitcnt vmcnt(5)
	v_add_u32_e32 v17, v17, v9
	s_waitcnt vmcnt(4)
	v_add_u32_e32 v17, v17, v10
	s_waitcnt vmcnt(3)
	v_add_u32_e32 v17, v17, v11
	s_waitcnt vmcnt(2)
	v_add_u32_e32 v17, v17, v12
	s_waitcnt vmcnt(1)
	v_add_u32_e32 v17, v17, v13
	s_waitcnt vmcnt(0)
	v_add_u32_e32 v17, v17, v14
	v_cmp_eq_u32_e32 vcc, s20, v17
	s_cbranch_vccnz .LBB0_3179
	s_and_b32 s12, s21, 0xff
	s_cmp_eq_u32 s12, 0
	s_mov_b64 s[12:13], -1
	s_mov_b64 s[16:17], -1
	s_nop 0
	s_cbranch_scc1 .LBB0_3184
	s_and_b64 vcc, exec, s[16:17]
	s_cbranch_vccz .LBB0_3179

.LBB0_3198:
	s_and_b32 s20, s24, 0xff
	s_mov_b64 s[16:17], -1
	s_cmp_lg_u32 s20, 0
	s_mov_b64 s[22:23], -1
	s_nop 0
	s_cbranch_scc0 .LBB0_3201
	s_and_b64 vcc, exec, s[22:23]
	s_cbranch_vccz .LBB0_3197

.LBB0_3215:
	s_and_b32 s20, s26, 0xff
	s_cmp_lg_u32 s20, 0
	s_mov_b64 s[22:23], -1
	s_nop 0
	s_cbranch_scc0 .LBB0_3218
	s_mov_b64 s[24:25], -1
	s_and_b64 vcc, exec, s[22:23]
	s_cbranch_vccz .LBB0_3214

.LBB0_3348:
	global_load_dword v15, v16, s[72:73] offset:1024 sc1
	global_load_dword v0, v16, s[72:73] offset:1280 sc1
	global_load_dword v1, v16, s[72:73] offset:1536 sc1
	global_load_dword v2, v16, s[72:73] offset:1792 sc1
	global_load_dword v3, v16, s[72:73] offset:2048 sc1
	global_load_dword v4, v16, s[72:73] offset:2304 sc1
	global_load_dword v5, v16, s[72:73] offset:2560 sc1
	global_load_dword v6, v16, s[72:73] offset:2816 sc1
	global_load_dword v7, v16, s[72:73] offset:3072 sc1
	global_load_dword v8, v16, s[72:73] offset:3328 sc1
	global_load_dword v9, v16, s[72:73] offset:3584 sc1
	global_load_dword v10, v16, s[72:73] offset:3840 sc1
	global_load_dword v11, v16, s[2:3] sc1
	global_load_dword v12, v16, s[4:5] sc1
	global_load_dword v13, v16, s[8:9] sc1
	global_load_dword v14, v16, s[10:11] sc1
	s_mov_b64 s[12:13], -1
	s_mov_b64 s[14:15], -1
	s_waitcnt vmcnt(14)
	v_add_u32_e32 v17, v0, v15
	s_waitcnt vmcnt(13)
	v_add_u32_e32 v17, v17, v1
	s_waitcnt vmcnt(12)
	v_add_u32_e32 v17, v17, v2
	s_waitcnt vmcnt(11)
	v_add_u32_e32 v17, v17, v3
	s_waitcnt vmcnt(10)
	v_add_u32_e32 v17, v17, v4
	s_waitcnt vmcnt(9)
	v_add_u32_e32 v17, v17, v5
	s_waitcnt vmcnt(8)
	v_add_u32_e32 v17, v17, v6
	s_waitcnt vmcnt(7)
	v_add_u32_e32 v17, v17, v7
	s_waitcnt vmcnt(6)
	v_add_u32_e32 v17, v17, v8
	s_waitcnt vmcnt(5)
	v_add_u32_e32 v17, v17, v9
	s_waitcnt vmcnt(4)
	v_add_u32_e32 v17, v17, v10
	s_waitcnt vmcnt(3)
	v_add_u32_e32 v17, v17, v11
	s_waitcnt vmcnt(2)
	v_add_u32_e32 v17, v17, v12
	s_waitcnt vmcnt(1)
	v_add_u32_e32 v17, v17, v13
	s_waitcnt vmcnt(0)
	v_add_u32_e32 v17, v17, v14
	v_cmp_eq_u32_e32 vcc, s22, v17
	s_cbranch_vccnz .LBB0_3347
	s_and_b32 s12, s23, 0xff
	s_cmp_eq_u32 s12, 0
	s_mov_b64 s[12:13], -1
	s_mov_b64 s[16:17], -1
	s_nop 0
	s_cbranch_scc1 .LBB0_3352
	s_and_b64 vcc, exec, s[16:17]
	s_cbranch_vccz .LBB0_3347

.LBB0_3366:
	s_and_b32 s22, s26, 0xff
	s_mov_b64 s[16:17], -1
	s_cmp_lg_u32 s22, 0
	s_mov_b64 s[24:25], -1
	s_nop 0
	s_cbranch_scc0 .LBB0_3369
	s_and_b64 vcc, exec, s[24:25]
	s_cbranch_vccz .LBB0_3365

.LBB0_3383:
	s_and_b32 s22, s28, 0xff
	s_cmp_lg_u32 s22, 0
	s_mov_b64 s[24:25], -1
	s_nop 0
	s_cbranch_scc0 .LBB0_3386
	s_mov_b64 s[26:27], -1
	s_and_b64 vcc, exec, s[24:25]
	s_cbranch_vccz .LBB0_3382

.LBB0_3438:
	global_load_dword v15, v16, s[72:73] offset:1024 sc1
	global_load_dword v0, v16, s[72:73] offset:1280 sc1
	global_load_dword v1, v16, s[72:73] offset:1536 sc1
	global_load_dword v2, v16, s[72:73] offset:1792 sc1
	global_load_dword v3, v16, s[72:73] offset:2048 sc1
	global_load_dword v4, v16, s[72:73] offset:2304 sc1
	global_load_dword v5, v16, s[72:73] offset:2560 sc1
	global_load_dword v6, v16, s[72:73] offset:2816 sc1
	global_load_dword v7, v16, s[72:73] offset:3072 sc1
	global_load_dword v8, v16, s[72:73] offset:3328 sc1
	global_load_dword v9, v16, s[72:73] offset:3584 sc1
	global_load_dword v10, v16, s[72:73] offset:3840 sc1
	global_load_dword v11, v16, s[4:5] sc1
	global_load_dword v12, v16, s[6:7] sc1
	global_load_dword v13, v16, s[8:9] sc1
	global_load_dword v14, v16, s[10:11] sc1
	s_mov_b64 s[12:13], -1
	s_mov_b64 s[14:15], -1
	s_waitcnt vmcnt(14)
	v_add_u32_e32 v17, v0, v15
	s_waitcnt vmcnt(13)
	v_add_u32_e32 v17, v17, v1
	s_waitcnt vmcnt(12)
	v_add_u32_e32 v17, v17, v2
	s_waitcnt vmcnt(11)
	v_add_u32_e32 v17, v17, v3
	s_waitcnt vmcnt(10)
	v_add_u32_e32 v17, v17, v4
	s_waitcnt vmcnt(9)
	v_add_u32_e32 v17, v17, v5
	s_waitcnt vmcnt(8)
	v_add_u32_e32 v17, v17, v6
	s_waitcnt vmcnt(7)
	v_add_u32_e32 v17, v17, v7
	s_waitcnt vmcnt(6)
	v_add_u32_e32 v17, v17, v8
	s_waitcnt vmcnt(5)
	v_add_u32_e32 v17, v17, v9
	s_waitcnt vmcnt(4)
	v_add_u32_e32 v17, v17, v10
	s_waitcnt vmcnt(3)
	v_add_u32_e32 v17, v17, v11
	s_waitcnt vmcnt(2)
	v_add_u32_e32 v17, v17, v12
	s_waitcnt vmcnt(1)
	v_add_u32_e32 v17, v17, v13
	s_waitcnt vmcnt(0)
	v_add_u32_e32 v17, v17, v14
	v_cmp_eq_u32_e32 vcc, s22, v17
	s_cbranch_vccnz .LBB0_3437
	s_and_b32 s12, s23, 0xff
	s_cmp_eq_u32 s12, 0
	s_mov_b64 s[12:13], -1
	s_mov_b64 s[16:17], -1
	s_nop 0
	s_cbranch_scc1 .LBB0_3442
	s_and_b64 vcc, exec, s[16:17]
	s_cbranch_vccz .LBB0_3437
